# baseline (speedup 1.0000x reference)
.LBB4_11:
	s_and_b32 s14, s15, 1
	global_load_dwordx4 v[112:115], v128, s[8:9]
	global_load_dwordx4 v[116:119], v204, s[8:9]
	global_load_dwordx4 v[120:123], v128, s[0:1]
	global_load_dwordx4 v[124:127], v204, s[0:1]
	s_add_i32 s15, s15, 1
	s_mul_i32 s18, s14, 0x2400
	v_add_u32_e32 v202, s18, v167
	ds_read_b128 v[80:83], v202
	ds_read_b128 v[190:193], v202 offset:32
	ds_read_b128 v[194:197], v202 offset:4608
	ds_read_b128 v[198:201], v202 offset:4640
	s_waitcnt lgkmcnt(3)
	v_mfma_f32_32x32x16_f16 v[64:79], v[108:111], v[80:83], v[48:63]
	s_waitcnt lgkmcnt(1)
	v_mfma_f32_32x32x16_f16 v[80:95], v[108:111], v[194:197], v[48:63]
	v_mfma_f32_32x32x16_f16 v[64:79], v[104:107], v[190:193], v[64:79]
	ds_read_b128 v[190:193], v202 offset:64
	ds_read_b128 v[194:197], v202 offset:96
	s_waitcnt lgkmcnt(2)
	v_mfma_f32_32x32x16_f16 v[80:95], v[104:107], v[198:201], v[80:95]
	s_waitcnt lgkmcnt(1)
	v_mfma_f32_32x32x16_f16 v[64:79], v[100:103], v[190:193], v[64:79]
	ds_read_b128 v[190:193], v202 offset:4672
	ds_read_b128 v[198:201], v202 offset:4704
	s_waitcnt lgkmcnt(1)
	v_mfma_f32_32x32x16_f16 v[80:95], v[100:103], v[190:193], v[80:95]
	v_mfma_f32_32x32x16_f16 v[64:79], v[96:99], v[194:197], v[64:79]
	s_waitcnt lgkmcnt(0)
	v_mfma_f32_32x32x16_f16 v[80:95], v[96:99], v[198:201], v[80:95]
	s_setprio 2
	s_add_u32 s8, s8, 0x2000
	s_addc_u32 s9, s9, 0
	s_add_u32 s0, s0, 0x2000
	s_addc_u32 s1, s1, 0
	s_nop 4
	v_exp_f32_e32 v192, v64
	s_nop 0
	v_exp_f32_e32 v80, v80
	v_exp_f32_e32 v193, v65
	v_exp_f32_e32 v81, v81
	v_mul_f32_e32 v64, v192, v183
	v_exp_f32_e32 v66, v66
	global_store_dword v132, v64, s[42:43] offset:-128
	v_mul_f32_e32 v64, v80, v183
	v_exp_f32_e32 v82, v82
	global_store_dword v132, v64, s[42:43]
	v_mul_f32_e32 v190, v193, v182
	v_exp_f32_e32 v67, v67
	global_store_dword v136, v190, s[42:43] offset:-128
	v_mul_f32_e32 v190, v81, v182
	v_exp_f32_e32 v83, v83
	global_store_dword v136, v190, s[42:43]
	v_mul_f32_e32 v190, v66, v181
	global_store_dword v140, v190, s[42:43] offset:-128
	v_mul_f32_e32 v190, v82, v181
	global_store_dword v140, v190, s[42:43]
	v_mul_f32_e32 v190, v67, v180
	global_store_dword v144, v190, s[42:43] offset:-128
	v_mul_f32_e32 v190, v83, v180
	global_store_dword v144, v190, s[42:43]
	v_exp_f32_e32 v190, v68
	v_cvt_pk_f16_f32 v65, v66, v67
	v_cvt_pk_f16_f32 v67, v82, v83
	v_exp_f32_e32 v82, v84
	v_cvt_pk_f16_f32 v66, v80, v81
	v_mul_f32_e32 v68, v190, v179
	global_store_dword v148, v68, s[42:43] offset:-128
	v_exp_f32_e32 v83, v69
	v_mul_f32_e32 v68, v82, v179
	global_store_dword v148, v68, s[42:43]
	v_exp_f32_e32 v80, v85
	v_mul_f32_e32 v81, v83, v178
	global_store_dword v152, v81, s[42:43] offset:-128
	v_exp_f32_e32 v70, v70
	v_mul_f32_e32 v81, v80, v178
	global_store_dword v152, v81, s[42:43]
	v_exp_f32_e32 v81, v86
	v_mul_f32_e32 v84, v70, v177
	global_store_dword v156, v84, s[42:43] offset:-128
	v_exp_f32_e32 v71, v71
	v_mul_f32_e32 v84, v81, v177
	global_store_dword v156, v84, s[42:43]
	v_exp_f32_e32 v84, v87
	v_mul_f32_e32 v85, v71, v176
	global_store_dword v160, v85, s[42:43] offset:-128
	v_mul_f32_e32 v85, v84, v176
	v_cvt_pk_f16_f32 v64, v192, v193
	global_store_dword v160, v85, s[42:43]
	v_cvt_pk_f16_f32 v69, v70, v71
	v_cvt_pk_f16_f32 v68, v190, v83
	v_exp_f32_e32 v72, v72
	v_cvt_pk_f16_f32 v71, v81, v84
	v_cvt_pk_f16_f32 v70, v82, v80
	ds_write2_b64 v187, v[64:65], v[68:69] offset1:2
	ds_write2_b64 v131, v[66:67], v[70:71] offset0:32 offset1:34
	v_exp_f32_e32 v66, v88
	v_mul_f32_e32 v67, v72, v175
	global_store_dword v162, v67, s[42:43]
	v_exp_f32_e32 v67, v73
	v_mul_f32_e32 v68, v66, v175
	global_store_dword v162, v68, s[42:43] offset:128
	v_exp_f32_e32 v68, v89
	v_mul_f32_e32 v69, v67, v174
	global_store_dword v158, v69, s[42:43]
	v_exp_f32_e32 v69, v74
	v_mul_f32_e32 v70, v68, v174
	global_store_dword v158, v70, s[42:43] offset:128
	v_exp_f32_e32 v70, v90
	v_mul_f32_e32 v71, v69, v173
	global_store_dword v154, v71, s[42:43]
	v_exp_f32_e32 v71, v75
	v_mul_f32_e32 v73, v70, v173
	global_store_dword v154, v73, s[42:43] offset:128
	v_exp_f32_e32 v73, v91
	v_mul_f32_e32 v74, v71, v172
	global_store_dword v150, v74, s[42:43]
	v_mul_f32_e32 v74, v73, v172
	global_store_dword v150, v74, s[42:43] offset:128
	v_cvt_pk_f16_f32 v65, v69, v71
	v_exp_f32_e32 v71, v76
	v_cvt_pk_f16_f32 v64, v72, v67
	v_cvt_pk_f16_f32 v67, v70, v73
	v_exp_f32_e32 v70, v92
	v_cvt_pk_f16_f32 v66, v66, v68
	v_mul_f32_e32 v72, v71, v171
	global_store_dword v146, v72, s[42:43]
	v_exp_f32_e32 v72, v77
	v_mul_f32_e32 v73, v70, v171
	global_store_dword v146, v73, s[42:43] offset:128
	v_exp_f32_e32 v73, v93
	v_mul_f32_e32 v74, v72, v170
	global_store_dword v142, v74, s[42:43]
	v_exp_f32_e32 v74, v78
	v_mul_f32_e32 v75, v73, v170
	global_store_dword v142, v75, s[42:43] offset:128
	v_exp_f32_e32 v75, v94
	v_mul_f32_e32 v76, v74, v169
	global_store_dword v138, v76, s[42:43]
	v_exp_f32_e32 v76, v79
	v_mul_f32_e32 v77, v75, v169
	global_store_dword v138, v77, s[42:43] offset:128
	v_exp_f32_e32 v77, v95
	v_mul_f32_e32 v78, v76, v168
	global_store_dword v134, v78, s[42:43]
	v_mul_f32_e32 v78, v77, v168
	global_store_dword v134, v78, s[42:43] offset:128
	v_cvt_pk_f16_f32 v69, v74, v76
	v_cvt_pk_f16_f32 v68, v71, v72
	v_cvt_pk_f16_f32 v71, v75, v77
	v_cvt_pk_f16_f32 v70, v70, v73
	ds_write2_b64 v187, v[64:65], v[68:69] offset0:4 offset1:6
	ds_write2_b64 v131, v[66:67], v[70:71] offset0:36 offset1:38
	s_setprio 0
	ds_read_b64_tr_b16 v[64:65], v186
	ds_read_b64_tr_b16 v[66:67], v186 offset:288
	s_mul_i32 s18, s14, 0x3000
	v_or_b32_e32 v80, s18, v185
	ds_read_b64_tr_b16 v[68:69], v80
	ds_read_b64_tr_b16 v[70:71], v80 offset:768
	ds_read_b64_tr_b16 v[74:75], v80 offset:832
	ds_read_b64_tr_b16 v[72:73], v80 offset:64
	ds_read_b64_tr_b16 v[76:77], v186 offset:1152
	ds_read_b64_tr_b16 v[78:79], v186 offset:1440
	s_waitcnt lgkmcnt(4)
	v_mfma_f32_32x32x16_f16 v[0:15], v[64:67], v[68:71], v[0:15]
	s_waitcnt lgkmcnt(2)
	v_mfma_f32_32x32x16_f16 v[16:31], v[64:67], v[72:75], v[16:31]
	ds_read_b64_tr_b16 v[64:65], v80 offset:3072
	ds_read_b64_tr_b16 v[66:67], v80 offset:3840
	ds_read_b64_tr_b16 v[70:71], v80 offset:3904
	ds_read_b64_tr_b16 v[68:69], v80 offset:3136
	s_waitcnt lgkmcnt(2)
	v_mfma_f32_32x32x16_f16 v[0:15], v[76:79], v[64:67], v[0:15]
	s_waitcnt lgkmcnt(0)
	v_mfma_f32_32x32x16_f16 v[16:31], v[76:79], v[68:71], v[16:31]
	ds_read_b64_tr_b16 v[64:65], v186 offset:2304
	ds_read_b64_tr_b16 v[66:67], v186 offset:2592
	ds_read_b64_tr_b16 v[68:69], v80 offset:6144
	ds_read_b64_tr_b16 v[70:71], v80 offset:6912
	ds_read_b64_tr_b16 v[74:75], v80 offset:6976
	ds_read_b64_tr_b16 v[72:73], v80 offset:6208
	ds_read_b64_tr_b16 v[76:77], v186 offset:3456
	ds_read_b64_tr_b16 v[78:79], v186 offset:3744
	s_waitcnt lgkmcnt(4)
	v_mfma_f32_32x32x16_f16 v[0:15], v[64:67], v[68:71], v[0:15]
	s_waitcnt lgkmcnt(2)
	v_mfma_f32_32x32x16_f16 v[16:31], v[64:67], v[72:75], v[16:31]
	ds_read_b64_tr_b16 v[64:65], v80 offset:9216
	ds_read_b64_tr_b16 v[66:67], v80 offset:9984
	ds_read_b64_tr_b16 v[70:71], v80 offset:10048
	ds_read_b64_tr_b16 v[68:69], v80 offset:9280
	s_waitcnt lgkmcnt(2)
	v_mfma_f32_32x32x16_f16 v[0:15], v[76:79], v[64:67], v[0:15]
	s_waitcnt lgkmcnt(0)
	v_mfma_f32_32x32x16_f16 v[16:31], v[76:79], v[68:71], v[16:31]
	s_xor_b32 s14, s14, 1
	s_mul_i32 s18, s14, 0x3000
	s_mulk_i32 s14, 0x2400
	s_addk_i32 s14, 0x6000
	s_add_u32 s10, s10, 0x100
	s_addc_u32 s11, s11, 0
	s_add_u32 s42, s42, 0x100
	s_addc_u32 s43, s43, 0
	v_lshl_add_u32 v67, v166, 1, s14
	s_cmpk_eq_i32 s10, 0x1f00
	v_lshl_add_u32 v64, v189, 1, s18
	v_lshl_add_u32 v65, v188, 1, s18
	v_lshl_add_u32 v66, v165, 1, s14
	s_waitcnt vmcnt(35)
	ds_write_b128 v67, v[112:115]
	s_waitcnt vmcnt(34)
	ds_write_b128 v66, v[116:119]
	s_waitcnt vmcnt(33)
	ds_write_b128 v65, v[120:123]
	s_waitcnt vmcnt(32)
	ds_write_b128 v64, v[124:127]
	s_waitcnt lgkmcnt(0)
	s_barrier
	s_cbranch_scc0 .LBB4_11
	s_lshl_b64 s[0:1], s[16:17], 13
	s_add_u32 s0, s4, s0
	s_addc_u32 s1, s5, s1
	v_xor_b32_e32 v52, 0x80000000, v34
	v_xor_b32_e32 v51, 0x80000000, v35
	v_xor_b32_e32 v50, 0x80000000, v32
	v_xor_b32_e32 v49, 0x80000000, v33
	ds_read_b128 v[32:35], v167 offset:9216
	v_xor_b32_e32 v59, 0x80000000, v43
	v_xor_b32_e32 v58, 0x80000000, v40
	v_xor_b32_e32 v57, 0x80000000, v41
	v_xor_b32_e32 v56, 0x80000000, v38
	v_xor_b32_e32 v55, 0x80000000, v39
	v_xor_b32_e32 v54, 0x80000000, v36
	v_xor_b32_e32 v53, 0x80000000, v37
	v_xor_b32_e32 v48, 0x80000000, v46
	v_xor_b32_e32 v47, 0x80000000, v47
	v_xor_b32_e32 v46, 0x80000000, v42
	v_xor_b32_e32 v45, 0x80000000, v45
	v_xor_b32_e32 v44, 0x80000000, v44
	ds_read_b128 v[36:39], v167 offset:9248
	s_add_u32 s0, s0, 0x1f00
	s_waitcnt lgkmcnt(1)
	v_mfma_f32_32x32x16_f16 v[60:75], v[108:111], v[32:35], v[44:59]
	ds_read_b128 v[32:35], v167 offset:13824
	ds_read_b128 v[40:43], v167 offset:13856
	s_addc_u32 s1, s1, 0
	s_waitcnt lgkmcnt(1)
	v_mfma_f32_32x32x16_f16 v[44:59], v[108:111], v[32:35], v[44:59]
	v_mfma_f32_32x32x16_f16 v[60:75], v[104:107], v[36:39], v[60:75]
	ds_read_b128 v[32:35], v167 offset:9280
	ds_read_b128 v[36:39], v167 offset:9312
	s_waitcnt lgkmcnt(2)
	v_mfma_f32_32x32x16_f16 v[44:59], v[104:107], v[40:43], v[44:59]
	s_waitcnt lgkmcnt(1)
	v_mfma_f32_32x32x16_f16 v[60:75], v[100:103], v[32:35], v[60:75]
	ds_read_b128 v[32:35], v167 offset:13888
	ds_read_b128 v[40:43], v167 offset:13920
	s_waitcnt lgkmcnt(1)
	v_mfma_f32_32x32x16_f16 v[44:59], v[100:103], v[32:35], v[44:59]
	v_mfma_f32_32x32x16_f16 v[60:75], v[96:99], v[36:39], v[60:75]
	s_waitcnt lgkmcnt(0)
	v_mfma_f32_32x32x16_f16 v[44:59], v[96:99], v[40:43], v[44:59]
	s_setprio 2
	s_nop 8
	v_exp_f32_e32 v32, v60
	s_nop 0
	v_exp_f32_e32 v34, v44
	v_exp_f32_e32 v35, v61
	v_or_b32_e32 v37, 0x2000, v130
	v_mul_f32_e32 v33, v32, v183
	v_mul_f32_e32 v36, v34, v183
	global_store_dword v130, v33, s[0:1]
	global_store_dword v130, v36, s[0:1] offset:128
	v_exp_f32_e32 v36, v45
	v_mul_f32_e32 v33, v35, v182
	global_store_dword v37, v33, s[0:1]
	v_exp_f32_e32 v33, v62
	v_mul_f32_e32 v38, v36, v182
	global_store_dword v37, v38, s[0:1] offset:128
	v_exp_f32_e32 v37, v46
	v_mul_f32_e32 v38, v33, v181
	v_or_b32_e32 v39, 0x4000, v130
	global_store_dword v39, v38, s[0:1]
	v_exp_f32_e32 v38, v63
	v_mul_f32_e32 v40, v37, v181
	global_store_dword v39, v40, s[0:1] offset:128
	v_exp_f32_e32 v39, v47
	v_mul_f32_e32 v40, v38, v180
	v_cvt_pk_f16_f32 v33, v33, v38
	v_exp_f32_e32 v38, v64
	v_or_b32_e32 v41, 0x6000, v130
	global_store_dword v41, v40, s[0:1]
	v_mul_f32_e32 v40, v39, v180
	global_store_dword v41, v40, s[0:1] offset:128
	v_cvt_pk_f16_f32 v32, v32, v35
	v_cvt_pk_f16_f32 v35, v37, v39
	v_cvt_pk_f16_f32 v34, v34, v36
	v_exp_f32_e32 v40, v48
	v_mul_f32_e32 v36, v38, v179
	v_or_b32_e32 v37, 0x10000, v130
	global_store_dword v37, v36, s[0:1]
	v_exp_f32_e32 v36, v65
	v_exp_f32_e32 v41, v49
	v_mul_f32_e32 v39, v40, v179
	global_store_dword v37, v39, s[0:1] offset:128
	v_mul_f32_e32 v37, v36, v178
	v_or_b32_e32 v39, 0x12000, v130
	global_store_dword v39, v37, s[0:1]
	v_exp_f32_e32 v37, v66
	v_mul_f32_e32 v42, v41, v178
	global_store_dword v39, v42, s[0:1] offset:128
	v_exp_f32_e32 v39, v50
	v_mul_f32_e32 v42, v37, v177
	v_or_b32_e32 v43, 0x14000, v130
	global_store_dword v43, v42, s[0:1]
	v_exp_f32_e32 v42, v67
	v_mul_f32_e32 v44, v39, v177
	global_store_dword v43, v44, s[0:1] offset:128
	v_exp_f32_e32 v43, v51
	v_cvt_pk_f16_f32 v37, v37, v42
	v_cvt_pk_f16_f32 v36, v38, v36
	v_cvt_pk_f16_f32 v38, v40, v41
	v_cvt_pk_f16_f32 v39, v39, v43
	ds_write2_b64 v187, v[32:33], v[36:37] offset1:2
	v_exp_f32_e32 v32, v68
	v_add_u32_e32 v40, 0x800, v187
	ds_write2_b64 v40, v[34:35], v[38:39] offset0:32 offset1:34
	v_exp_f32_e32 v34, v52
	v_exp_f32_e32 v36, v69
	v_exp_f32_e32 v37, v53
	v_mul_f32_e32 v33, v32, v175
	v_or_b32_e32 v35, 0x20000, v130
	global_store_dword v35, v33, s[0:1]
	v_mul_f32_e32 v33, v34, v175
	global_store_dword v35, v33, s[0:1] offset:128
	v_mul_f32_e32 v33, v36, v174
	v_or_b32_e32 v35, 0x22000, v130
	global_store_dword v35, v33, s[0:1]
	v_exp_f32_e32 v33, v70
	v_mul_f32_e32 v38, v37, v174
	global_store_dword v35, v38, s[0:1] offset:128
	v_exp_f32_e32 v35, v54
	v_mul_f32_e32 v38, v33, v173
	v_or_b32_e32 v39, 0x24000, v130
	global_store_dword v39, v38, s[0:1]
	v_exp_f32_e32 v38, v71
	v_mul_f32_e32 v41, v35, v173
	global_store_dword v39, v41, s[0:1] offset:128
	v_exp_f32_e32 v39, v55
	v_mul_f32_e32 v44, v42, v176
	v_mul_f32_e32 v41, v38, v172
	v_or_b32_e32 v42, 0x26000, v130
	v_cvt_pk_f16_f32 v32, v32, v36
	v_exp_f32_e32 v36, v72
	global_store_dword v42, v41, s[0:1]
	v_mul_f32_e32 v41, v39, v172
	v_cvt_pk_f16_f32 v33, v33, v38
	v_exp_f32_e32 v38, v56
	global_store_dword v42, v41, s[0:1] offset:128
	v_exp_f32_e32 v41, v73
	v_exp_f32_e32 v42, v57
	v_cvt_pk_f16_f32 v35, v35, v39
	v_cvt_pk_f16_f32 v34, v34, v37
	v_mul_f32_e32 v37, v36, v171
	v_or_b32_e32 v39, 0x30000, v130
	global_store_dword v39, v37, s[0:1]
	v_mul_f32_e32 v37, v38, v171
	v_or_b32_e32 v45, 0x16000, v130
	global_store_dword v39, v37, s[0:1] offset:128
	v_mul_f32_e32 v37, v41, v170
	v_or_b32_e32 v39, 0x32000, v130
	global_store_dword v45, v44, s[0:1]
	v_mul_f32_e32 v44, v43, v176
	global_store_dword v39, v37, s[0:1]
	v_exp_f32_e32 v37, v74
	v_mul_f32_e32 v43, v42, v170
	global_store_dword v39, v43, s[0:1] offset:128
	v_exp_f32_e32 v39, v58
	global_store_dword v45, v44, s[0:1] offset:128
	v_mul_f32_e32 v43, v37, v169
	v_or_b32_e32 v44, 0x34000, v130
	global_store_dword v44, v43, s[0:1]
	v_exp_f32_e32 v43, v75
	v_mul_f32_e32 v45, v39, v169
	global_store_dword v44, v45, s[0:1] offset:128
	v_exp_f32_e32 v44, v59
	v_mul_f32_e32 v45, v43, v168
	v_or_b32_e32 v46, 0x36000, v130
	global_store_dword v46, v45, s[0:1]
	v_mul_f32_e32 v45, v44, v168
	v_cvt_pk_f16_f32 v37, v37, v43
	v_cvt_pk_f16_f32 v36, v36, v41
	global_store_dword v46, v45, s[0:1] offset:128
	v_cvt_pk_f16_f32 v39, v39, v44
	v_cvt_pk_f16_f32 v38, v38, v42
	ds_write2_b64 v187, v[32:33], v[36:37] offset0:4 offset1:6
	ds_write2_b64 v40, v[34:35], v[38:39] offset0:36 offset1:38
	s_setprio 0
	ds_read_b64_tr_b16 v[32:33], v186
	ds_read_b64_tr_b16 v[34:35], v186 offset:288
	ds_read_b64_tr_b16 v[36:37], v185 offset:12288
	ds_read_b64_tr_b16 v[38:39], v185 offset:13056
	ds_read_b64_tr_b16 v[42:43], v185 offset:13120
	ds_read_b64_tr_b16 v[40:41], v185 offset:12352
	ds_read_b64_tr_b16 v[44:45], v186 offset:1152
	ds_read_b64_tr_b16 v[46:47], v186 offset:1440
	s_waitcnt lgkmcnt(4)
	v_mfma_f32_32x32x16_f16 v[0:15], v[32:35], v[36:39], v[0:15]
	s_waitcnt lgkmcnt(2)
	v_mfma_f32_32x32x16_f16 v[16:31], v[32:35], v[40:43], v[16:31]
	ds_read_b64_tr_b16 v[32:33], v185 offset:15360
	ds_read_b64_tr_b16 v[34:35], v185 offset:16128
	ds_read_b64_tr_b16 v[38:39], v185 offset:16192
	ds_read_b64_tr_b16 v[36:37], v185 offset:15424
	s_waitcnt lgkmcnt(2)
	v_mfma_f32_32x32x16_f16 v[0:15], v[44:47], v[32:35], v[0:15]
	s_waitcnt lgkmcnt(0)
	v_mfma_f32_32x32x16_f16 v[16:31], v[44:47], v[36:39], v[16:31]
	ds_read_b64_tr_b16 v[32:33], v186 offset:2304
	ds_read_b64_tr_b16 v[34:35], v186 offset:2592
	ds_read_b64_tr_b16 v[36:37], v185 offset:18432
	ds_read_b64_tr_b16 v[38:39], v185 offset:19200
	ds_read_b64_tr_b16 v[42:43], v185 offset:19264
	ds_read_b64_tr_b16 v[40:41], v185 offset:18496
	ds_read_b64_tr_b16 v[44:45], v186 offset:3456
	ds_read_b64_tr_b16 v[46:47], v186 offset:3744
	s_waitcnt lgkmcnt(4)
	v_mfma_f32_32x32x16_f16 v[0:15], v[32:35], v[36:39], v[0:15]
	s_waitcnt lgkmcnt(2)
	v_mfma_f32_32x32x16_f16 v[16:31], v[32:35], v[40:43], v[16:31]
	ds_read_b64_tr_b16 v[32:33], v185 offset:21504
	ds_read_b64_tr_b16 v[34:35], v185 offset:22272
	ds_read_b64_tr_b16 v[38:39], v185 offset:22336
	ds_read_b64_tr_b16 v[36:37], v185 offset:21568
	s_waitcnt lgkmcnt(2)
	v_mfma_f32_32x32x16_f16 v[0:15], v[44:47], v[32:35], v[0:15]
	s_waitcnt lgkmcnt(0)
	v_mfma_f32_32x32x16_f16 v[16:31], v[44:47], v[36:39], v[16:31]
	s_lshl_b32 s0, s2, 3
	s_and_b32 s0, s0, 0x7ffff800
	s_add_i32 s3, s3, s0
	s_lshl_b32 s0, s12, 7
	s_and_b32 s0, s0, 0x780
	s_add_u32 s0, s6, s0
	s_addc_u32 s1, s7, 0
	v_or_b32_e32 v32, s3, v184
	v_lshlrev_b32_e32 v34, 1, v164
	v_lshl_add_u32 v36, v32, 11, v34
	s_add_u32 s44, s0, 0x1000
	s_addc_u32 s45, s1, 0
	s_add_u32 s46, s44, 0x4000
	s_addc_u32 s47, s45, 0
	s_add_u32 s48, s46, 0x4000
	s_addc_u32 s49, s47, 0
	s_add_u32 s50, s48, 0x4000
	s_addc_u32 s51, s49, 0
	s_waitcnt vmcnt(63) expcnt(7) lgkmcnt(15)
	s_barrier
	v_fma_mixlo_f16 v38, v0, v183, 0
	global_store_short v36, v38, s[44:45] offset:-4096
	v_fma_mixlo_f16 v39, v16, v183, 0
	global_store_short v36, v39, s[44:45] offset:-4032
	v_fma_mixlo_f16 v40, v1, v182, 0
	global_store_short v36, v40, s[44:45] offset:-2048
	v_fma_mixlo_f16 v41, v17, v182, 0
	global_store_short v36, v41, s[44:45] offset:-1984
	v_fma_mixlo_f16 v38, v2, v181, 0
	global_store_short v36, v38, s[44:45]
	v_fma_mixlo_f16 v39, v18, v181, 0
	global_store_short v36, v39, s[44:45] offset:64
	v_fma_mixlo_f16 v40, v3, v180, 0
	global_store_short v36, v40, s[44:45] offset:2048
	v_fma_mixlo_f16 v41, v19, v180, 0
	global_store_short v36, v41, s[44:45] offset:2112
	v_fma_mixlo_f16 v38, v4, v179, 0
	global_store_short v36, v38, s[46:47] offset:-4096
	v_fma_mixlo_f16 v39, v20, v179, 0
	global_store_short v36, v39, s[46:47] offset:-4032
	v_fma_mixlo_f16 v40, v5, v178, 0
	global_store_short v36, v40, s[46:47] offset:-2048
	v_fma_mixlo_f16 v41, v21, v178, 0
	global_store_short v36, v41, s[46:47] offset:-1984
	v_fma_mixlo_f16 v38, v6, v177, 0
	global_store_short v36, v38, s[46:47]
	v_fma_mixlo_f16 v39, v22, v177, 0
	global_store_short v36, v39, s[46:47] offset:64
	v_fma_mixlo_f16 v40, v7, v176, 0
	global_store_short v36, v40, s[46:47] offset:2048
	v_fma_mixlo_f16 v41, v23, v176, 0
	global_store_short v36, v41, s[46:47] offset:2112
	v_fma_mixlo_f16 v38, v8, v175, 0
	global_store_short v36, v38, s[48:49] offset:-4096
	v_fma_mixlo_f16 v39, v24, v175, 0
	global_store_short v36, v39, s[48:49] offset:-4032
	v_fma_mixlo_f16 v40, v9, v174, 0
	global_store_short v36, v40, s[48:49] offset:-2048
	v_fma_mixlo_f16 v41, v25, v174, 0
	global_store_short v36, v41, s[48:49] offset:-1984
	v_fma_mixlo_f16 v38, v10, v173, 0
	global_store_short v36, v38, s[48:49]
	v_fma_mixlo_f16 v39, v26, v173, 0
	global_store_short v36, v39, s[48:49] offset:64
	v_fma_mixlo_f16 v40, v11, v172, 0
	global_store_short v36, v40, s[48:49] offset:2048
	v_fma_mixlo_f16 v41, v27, v172, 0
	global_store_short v36, v41, s[48:49] offset:2112
	v_fma_mixlo_f16 v38, v12, v171, 0
	global_store_short v36, v38, s[50:51] offset:-4096
	v_fma_mixlo_f16 v39, v28, v171, 0
	global_store_short v36, v39, s[50:51] offset:-4032
	v_fma_mixlo_f16 v40, v13, v170, 0
	global_store_short v36, v40, s[50:51] offset:-2048
	v_fma_mixlo_f16 v41, v29, v170, 0
	global_store_short v36, v41, s[50:51] offset:-1984
	v_fma_mixlo_f16 v38, v14, v169, 0
	global_store_short v36, v38, s[50:51]
	v_fma_mixlo_f16 v39, v30, v169, 0
	global_store_short v36, v39, s[50:51] offset:64
	v_fma_mixlo_f16 v40, v15, v168, 0
	global_store_short v36, v40, s[50:51] offset:2048
	v_fma_mixlo_f16 v41, v31, v168, 0
	global_store_short v36, v41, s[50:51] offset:2112
	s_endpgm
	.p2alignl 8, 3212836864
